# adds attention: v_permlane32_swap instead of ds_bpermute for the cross-half max and row-sum exchanges
# baseline (speedup 1.0000x reference)
;     ...
;                 mx = fmaxf(mx, __shfl_xor(mx, 32));
;                 const float mnew = fmaxf(mrun, mx); const bool grew = __any(mnew > mrun);
;                 if (grew) {
;                     const float alpha = __builtin_amdgcn_exp2f((mrun - mnew) * L2E);
;                     ls0 *= alpha; ls1 *= alpha; ls2 *= alpha; ls3 *= alpha;
; #pragma unroll
;                     for (int i = 0; i < 16; ++i) { oacc[0][i] *= alpha; oacc[1][i] *= alpha; } }
;                 mrun = mnew;
.LBB0_2233:
	v_mov_b32_e32 v32, v64
	s_nop 1
	v_permlane32_swap_b32_e32 v32, v64
	v_max3_f32 v32, v202, v64, v32
	v_cmp_gt_f32_e32 vcc, v32, v202
	s_cbranch_vccz .LBB0_2235
	v_sub_f32_e32 v33, v202, v32
	v_mul_f32_e32 v33, 0x3fb8aa3b, v33
	v_exp_f32_e32 v34, v33
	s_nop 0
	v_pk_mul_f32 v[30:31], v[30:31], v[34:35] op_sel_hi:[1,0]
	v_pk_mul_f32 v[28:29], v[28:29], v[34:35] op_sel_hi:[1,0]
	v_pk_mul_f32 v[26:27], v[26:27], v[34:35] op_sel_hi:[1,0]
	v_pk_mul_f32 v[24:25], v[24:25], v[34:35] op_sel_hi:[1,0]
	v_pk_mul_f32 v[22:23], v[22:23], v[34:35] op_sel_hi:[1,0]
	v_pk_mul_f32 v[20:21], v[20:21], v[34:35] op_sel_hi:[1,0]
	v_pk_mul_f32 v[18:19], v[18:19], v[34:35] op_sel_hi:[1,0]
	v_pk_mul_f32 v[16:17], v[16:17], v[34:35] op_sel_hi:[1,0]
	v_pk_mul_f32 v[14:15], v[14:15], v[34:35] op_sel_hi:[1,0]
	v_pk_mul_f32 v[12:13], v[12:13], v[34:35] op_sel_hi:[1,0]
	v_pk_mul_f32 v[10:11], v[10:11], v[34:35] op_sel_hi:[1,0]
	v_pk_mul_f32 v[8:9], v[8:9], v[34:35] op_sel_hi:[1,0]
	v_pk_mul_f32 v[6:7], v[6:7], v[34:35] op_sel_hi:[1,0]
	v_pk_mul_f32 v[4:5], v[4:5], v[34:35] op_sel_hi:[1,0]
	v_pk_mul_f32 v[2:3], v[2:3], v[34:35] op_sel_hi:[1,0]
	v_pk_mul_f32 v[0:1], v[0:1], v[34:35] op_sel_hi:[1,0]
	v_pk_mul_f32 v[120:121], v[120:121], v[34:35] op_sel_hi:[1,0]
	v_pk_mul_f32 v[118:119], v[118:119], v[34:35] op_sel_hi:[1,0]

; DI unsigned pk2(float lo, float hi) { f32x2 v = {lo, hi}; return __builtin_bit_cast(unsigned, __builtin_convertvector(v, bf16v2)); }
;     ...
;             float lsum = (ls0 + ls1) + (ls2 + ls3);
; #pragma unroll
;             for (int kk = 0; kk < 4; ++kk) asm volatile("" : "+v"(qfn[kk]));
;             asm volatile("" : "+v"(enn));
;             const float mx = mrun;
;             lsum += __shfl_xor(lsum, 32);
;             const float inv = 1.0f / lsum;
;             if (valid) {
;                 int hf = half; asm volatile("" : "+v"(hf));
;                 bf16_t* op = PO + ((size_t)slot * T + tok) * CW + h * 64 + 4 * hf;
; #pragma unroll
;                 for (int dt = 0; dt < 2; ++dt)
; #pragma unroll
;                     for (int ig = 0; ig < 4; ++ig) { u32x2 w; w.x = pk2(oacc[dt][4 * ig] * inv, oacc[dt][4 * ig + 1] * inv); w.y = pk2(oacc[dt][4 * ig + 2] * inv, oacc[dt][4 * ig + 3] * inv);
;                         *(u32x2*)(op + 32 * dt + 8 * ig) = w; }
;                 if (half == 0) PST[((size_t)slot * T + tok) * 8 + h] = (f32x2){mx, lsum};
.LBB0_2238:
	v_lshl_or_b32 v33, s20, 5, v149
	v_cmp_lt_i32_e32 vcc, v33, v245
	v_add_f32_e32 v33, v120, v121
	s_waitcnt lgkmcnt(0)
	v_add_f32_e32 v34, v118, v119
	v_add_f32_e32 v33, v34, v33
	s_nop 0
	v_mov_b32_e32 v34, v33
	s_nop 1
	v_permlane32_swap_b32_e32 v34, v33
	s_waitcnt vmcnt(3)
	s_waitcnt vmcnt(2)
	s_waitcnt vmcnt(1)
	s_waitcnt vmcnt(0)
	s_and_saveexec_b64 s[6:7], vcc
	s_cbranch_execz .LBB0_2225
	s_waitcnt lgkmcnt(0)
	v_add_f32_e32 v33, v33, v34
	v_div_scale_f32 v34, s[20:21], v33, v33, 1.0
	v_rcp_f32_e32 v35, v34
	v_div_scale_f32 v36, vcc, 1.0, v33, 1.0
	v_fma_f32 v37, -v34, v35, 1.0
	v_fmac_f32_e32 v35, v37, v35
	v_mul_f32_e32 v37, v36, v35
	v_fma_f32 v38, -v34, v37, v36
	v_fmac_f32_e32 v37, v38, v35
	v_fma_f32 v34, -v34, v37, v36
	v_mov_b32_e32 v36, 15
	v_lshlrev_b32_sdwa v36, v36, v248 dst_sel:DWORD dst_unused:UNUSED_PAD src0_sel:DWORD src1_sel:WORD_1
	v_div_fmas_f32 v34, v34, v35, v37
	v_mov_b32_e32 v35, v151
	v_add3_u32 v64, v249, s44, v36
	v_div_fixup_f32 v34, v34, v33, 1.0
	v_lshlrev_b64 v[36:37], 10, v[64:65]
	v_lshlrev_b32_e32 v38, 2, v35
	v_lshl_add_u64 v[36:37], s[0:1], 0, v[36:37]
	v_ashrrev_i32_e32 v39, 31, v38
	v_pk_mul_f32 v[16:17], v[16:17], v[34:35] op_sel_hi:[1,0]
	v_pk_mul_f32 v[18:19], v[18:19], v[34:35] op_sel_hi:[1,0]
	v_pk_mul_f32 v[0:1], v[0:1], v[34:35] op_sel_hi:[1,0]
	v_pk_mul_f32 v[2:3], v[2:3], v[34:35] op_sel_hi:[1,0]
	v_lshl_add_u64 v[36:37], v[38:39], 1, v[36:37]
	v_cvt_pk_bf16_f32 v16, v16, v17
	v_cvt_pk_bf16_f32 v17, v18, v19
	v_cvt_pk_bf16_f32 v0, v0, v1
	v_cvt_pk_bf16_f32 v1, v2, v3
	global_store_dwordx2 v[36:37], v[16:17], off
	v_pk_mul_f32 v[16:17], v[20:21], v[34:35] op_sel_hi:[1,0]
	v_pk_mul_f32 v[18:19], v[22:23], v[34:35] op_sel_hi:[1,0]
	global_store_dwordx2 v[36:37], v[0:1], off offset:64
	v_pk_mul_f32 v[0:1], v[4:5], v[34:35] op_sel_hi:[1,0]
	v_pk_mul_f32 v[2:3], v[6:7], v[34:35] op_sel_hi:[1,0]
	v_cvt_pk_bf16_f32 v16, v16, v17
	v_cvt_pk_bf16_f32 v17, v18, v19
	v_cvt_pk_bf16_f32 v0, v0, v1
	v_cvt_pk_bf16_f32 v1, v2, v3
	global_store_dwordx2 v[36:37], v[16:17], off offset:16
	v_pk_mul_f32 v[16:17], v[24:25], v[34:35] op_sel_hi:[1,0]
	v_pk_mul_f32 v[18:19], v[26:27], v[34:35] op_sel_hi:[1,0]
	global_store_dwordx2 v[36:37], v[0:1], off offset:80
	v_pk_mul_f32 v[0:1], v[8:9], v[34:35] op_sel_hi:[1,0]
	v_pk_mul_f32 v[2:3], v[10:11], v[34:35] op_sel_hi:[1,0]
	v_cvt_pk_bf16_f32 v16, v16, v17
	v_cvt_pk_bf16_f32 v17, v18, v19
	v_cvt_pk_bf16_f32 v0, v0, v1
	v_cvt_pk_bf16_f32 v1, v2, v3
	global_store_dwordx2 v[36:37], v[16:17], off offset:32
	v_pk_mul_f32 v[16:17], v[28:29], v[34:35] op_sel_hi:[1,0]
	v_pk_mul_f32 v[18:19], v[30:31], v[34:35] op_sel_hi:[1,0]
	global_store_dwordx2 v[36:37], v[0:1], off offset:96
	v_pk_mul_f32 v[0:1], v[12:13], v[34:35] op_sel_hi:[1,0]
	v_pk_mul_f32 v[2:3], v[14:15], v[34:35] op_sel_hi:[1,0]
	v_cvt_pk_bf16_f32 v16, v16, v17
	v_cvt_pk_bf16_f32 v17, v18, v19
	v_cvt_pk_bf16_f32 v0, v0, v1
	v_cvt_pk_bf16_f32 v1, v2, v3
	global_store_dwordx2 v[36:37], v[16:17], off offset:48
	global_store_dwordx2 v[36:37], v[0:1], off offset:112
	s_and_b64 exec, exec, s[12:13]
	s_cbranch_execz .LBB0_2225
	v_lshlrev_b64 v[0:1], 6, v[64:65]
	v_lshl_add_u64 v[0:1], s[2:3], 0, v[0:1]
	global_store_dwordx2 v[0:1], v[32:33], off
	s_branch .LBB0_2225
